# v050 + peer loop per-token absmax wave reduction via DPP instead of ds_bpermute chain
# speedup vs baseline: 1.0045x; 1.0032x over previous
; #define LAS __attribute__((address_space(3)))
; __device__ __forceinline__ void peer_stage_lists(const PeerMeta& m, LAS int* es, LAS unsigned* crep, LAS float* scp, int lane) {
;     es[lane] = m.e[0] << 8; es[64 + lane] = m.e[1] << 8;
;     const float cmax = wave_max(fmaxf(fabsf(m.c[0]), fabsf(m.c[1])));
;     const float inv = cmax > 0.f ? 127.0f / cmax : 0.f;
;     if (lane == 0) scp[0] = cmax * (1.0f / 127.0f);
; #pragma unroll
;     for (int hh = 0; hh < 2; ++hh) {
;         const int h = (int)rintf(m.c[hh] * inv);
;         crep[hh * 64 + (lane & 3) * 16 + (lane >> 2)] = (unsigned)(h & 255) * 0x01010101u;
;     }
; }
; __device__ __forceinline__ void acc_half_sel(i32x4 (&av)[4], const u32x4 (&R)[16], const LAS unsigned* cr  , int r, const unsigned (&mk)[4]) {
;     u32x4 c4[4];
; #pragma unroll
;     for (int q = 0; q < 4; ++q) c4[q] = *(const LAS u32x4*)(cr + r * 16 + 4 * q);
; #pragma unroll
;     for (int it = 0; it < 16; ++it) {
;         const unsigned rep = (it & 3) == 0 ? c4[it >> 2].x : (it & 3) == 1 ? c4[it >> 2].y : (it & 3) == 2 ? c4[it >> 2].z : c4[it >> 2].w;
;         i32x4 Aop; Aop.x = (int)(rep & mk[0]); Aop.y = (int)(rep & mk[1]); Aop.z = (int)(rep & mk[2]); Aop.w = (int)(rep & mk[3]);
;         av[it & 3] = __builtin_amdgcn_mfma_i32_16x16x64_i8(Aop, __builtin_bit_cast(i32x4, R[it]), av[it & 3], 0, 0, 0);
;     }
.LBB0_946:
	s_waitcnt vmcnt(39)
	v_lshlrev_b32_e32 v171, 8, v171
	s_waitcnt vmcnt(38)
	v_lshlrev_b32_e32 v172, 8, v172
	ds_write2st64_b32 v154, v171, v172 offset0:2 offset1:3
	s_waitcnt vmcnt(36)
	v_max_f32_e64 v171, |v165|, |v165|
	v_max_f32_e64 v172, |v166|, |v166|
	v_max_f32_e32 v171, v172, v171
	s_nop 1
	v_max_f32_dpp v171, v171, v171 quad_perm:[1,0,3,2] row_mask:0xf bank_mask:0xf
	s_nop 1
	v_max_f32_dpp v171, v171, v171 quad_perm:[2,3,0,1] row_mask:0xf bank_mask:0xf
	s_nop 1
	v_max_f32_dpp v171, v171, v171 row_half_mirror row_mask:0xf bank_mask:0xf
	s_nop 1
	v_max_f32_dpp v171, v171, v171 row_mirror row_mask:0xf bank_mask:0xf
	s_nop 1
	v_max_f32_dpp v171, v171, v171 row_bcast:15 row_mask:0xa bank_mask:0xf
	s_nop 1
	v_max_f32_dpp v171, v171, v171 row_bcast:31 row_mask:0xc bank_mask:0xf
	s_nop 1
	v_readlane_b32 s98, v171, 63
	s_nop 1
	v_mov_b32_e32 v171, s98
	v_max_f32_e32 v172, v171, v171
	s_and_saveexec_b64 s[6:7], s[2:3]
	v_mul_f32_e32 v172, 0x3c010204, v171
	v_mov_b32_e32 v173, s11
	ds_write_b32 v173, v172 offset:2052
	s_or_b64 exec, exec, s[6:7]
	v_div_scale_f32 v172, s[6:7], v171, v171, s12
	v_rcp_f32_e32 v173, v172
	v_div_scale_f32 v174, vcc, s12, v171, s12
	s_add_i32 s6, s14, 3
	v_fma_f32 v175, -v172, v173, 1.0
	v_fmac_f32_e32 v173, v175, v173
	v_mul_f32_e32 v175, v174, v173
	v_fma_f32 v176, -v172, v175, v174
	v_fmac_f32_e32 v175, v176, v173
	v_fma_f32 v172, -v172, v175, v174
	v_div_fmas_f32 v172, v172, v173, v175
	v_div_fixup_f32 v172, v172, v171, s12
	v_cmp_lt_f32_e32 vcc, 0, v171
	s_min_i32 s6, s6, s1
	s_mul_i32 s6, s6, s54
	v_cndmask_b32_e32 v171, 0, v172, vcc
	v_mul_f32_e32 v166, v166, v171
	v_mul_f32_e32 v165, v165, v171
	v_rndne_f32_e32 v166, v166
	v_rndne_f32_e32 v165, v165
	v_cvt_i32_f32_e32 v166, v166
	v_cvt_i32_f32_e32 v165, v165
	s_add_i32 s6, s6, s0
	s_ashr_i32 s7, s6, 31
	v_and_b32_e32 v166, 0xff, v166
	v_and_b32_e32 v165, 0xff, v165
	v_mul_lo_u32 v166, v166, s13
	v_mul_lo_u32 v165, v165, s13
	ds_write2st64_b32 v161, v166, v165 offset0:6 offset1:7
	ds_read_b128 v[172:175], v163 offset:1024
	s_lshl_b64 s[6:7], s[6:7], 9
	s_ashr_i32 s41, s40, 31
	s_waitcnt vmcnt(35)
	v_lshlrev_b32_e32 v169, 8, v169
	s_waitcnt vmcnt(34)
	v_lshlrev_b32_e32 v170, 8, v170
	s_waitcnt lgkmcnt(0)
	v_and_b32_e32 v176, v172, v1
	v_and_b32_e32 v177, v172, v150
	v_and_b32_e32 v178, v172, v151
	v_and_b32_e32 v179, v172, v152
	v_and_b32_e32 v180, v173, v1
	v_and_b32_e32 v181, v173, v150
	s_waitcnt vmcnt(31)
	v_mfma_i32_16x16x64_i8 v[82:85], v[176:179], v[82:85], 0
	v_and_b32_e32 v176, v174, v1
	v_and_b32_e32 v177, v174, v150
	v_and_b32_e32 v178, v174, v151
	v_and_b32_e32 v179, v174, v152
	v_and_b32_e32 v182, v173, v151
	v_and_b32_e32 v183, v173, v152
	s_waitcnt vmcnt(29)
	v_mfma_i32_16x16x64_i8 v[98:101], v[176:179], v[98:101], 0
	v_and_b32_e32 v172, v175, v1
	v_and_b32_e32 v173, v175, v150
	v_and_b32_e32 v174, v175, v151
	v_and_b32_e32 v175, v175, v152
	ds_read_b128 v[176:179], v163 offset:1040
	v_mfma_i32_16x16x64_i8 v[74:77], v[180:183], v[74:77], 0
	s_waitcnt vmcnt(28)
	v_mfma_i32_16x16x64_i8 v[38:41], v[172:175], v[38:41], 0
	s_waitcnt lgkmcnt(0)
	v_and_b32_e32 v172, v176, v1
	v_and_b32_e32 v173, v176, v150
	v_and_b32_e32 v174, v176, v151
	v_and_b32_e32 v175, v176, v152
	s_waitcnt vmcnt(27)
	s_nop 0
	v_mfma_i32_16x16x64_i8 v[50:53], v[172:175], v[50:53], v[82:85]
	v_mov_b32_e32 v173, s11
	s_nop 1
	v_and_b32_e32 v82, v177, v1
	v_and_b32_e32 v83, v177, v150
	v_and_b32_e32 v84, v177, v151
	v_and_b32_e32 v85, v177, v152
	s_waitcnt vmcnt(26)
	s_nop 0
	v_mfma_i32_16x16x64_i8 v[34:37], v[82:85], v[34:37], v[74:77]
	ds_read_b128 v[82:85], v163 offset:1056
	s_nop 1
	v_and_b32_e32 v74, v178, v1
	v_and_b32_e32 v75, v178, v150
	v_and_b32_e32 v76, v178, v151
	v_and_b32_e32 v77, v178, v152
	s_waitcnt vmcnt(25)
	s_nop 0
	v_mfma_i32_16x16x64_i8 v[54:57], v[74:77], v[54:57], v[98:101]
	v_and_b32_e32 v74, v179, v1
	v_and_b32_e32 v75, v179, v150
	v_and_b32_e32 v76, v179, v151
	v_and_b32_e32 v77, v179, v152
	s_waitcnt vmcnt(24)
	s_nop 0
	v_mfma_i32_16x16x64_i8 v[26:29], v[74:77], v[26:29], v[38:41]
	s_waitcnt lgkmcnt(0)
	s_nop 1
	v_and_b32_e32 v38, v82, v1
	v_and_b32_e32 v39, v82, v150
	v_and_b32_e32 v40, v82, v151
	v_and_b32_e32 v41, v82, v152
	s_waitcnt vmcnt(23)
	s_nop 0
	v_mfma_i32_16x16x64_i8 v[38:41], v[38:41], v[46:49], v[50:53]
	v_and_b32_e32 v46, v83, v1
	v_and_b32_e32 v47, v83, v150
	v_and_b32_e32 v48, v83, v151
	v_and_b32_e32 v49, v83, v152
	v_and_b32_e32 v50, v84, v1
	v_and_b32_e32 v51, v84, v150
	v_and_b32_e32 v52, v84, v151
	v_and_b32_e32 v53, v84, v152
	s_waitcnt vmcnt(22)
	v_mfma_i32_16x16x64_i8 v[30:33], v[46:49], v[30:33], v[34:37]
	v_and_b32_e32 v46, v85, v1
	v_and_b32_e32 v47, v85, v150
	v_and_b32_e32 v48, v85, v151
	ds_read_b128 v[34:37], v163 offset:1072
	v_and_b32_e32 v49, v85, v152
	s_waitcnt vmcnt(21)
	v_mfma_i32_16x16x64_i8 v[22:25], v[50:53], v[22:25], v[54:57]
	s_waitcnt lgkmcnt(0)
	v_and_b32_e32 v50, v34, v1
	v_and_b32_e32 v51, v34, v150
	v_and_b32_e32 v52, v34, v151
	v_and_b32_e32 v53, v34, v152
	s_waitcnt vmcnt(20)
	v_mfma_i32_16x16x64_i8 v[14:17], v[46:49], v[14:17], v[26:29]
	s_nop 2
	v_and_b32_e32 v26, v36, v1
	v_and_b32_e32 v27, v36, v150
	v_and_b32_e32 v28, v36, v151
	v_and_b32_e32 v29, v36, v152
	s_waitcnt vmcnt(19)
	v_mfma_i32_16x16x64_i8 v[174:177], v[50:53], v[18:21], v[38:41]
	v_and_b32_e32 v18, v35, v1
	v_and_b32_e32 v19, v35, v150
	v_and_b32_e32 v20, v35, v151
	v_and_b32_e32 v21, v35, v152
	s_waitcnt vmcnt(17)
	v_mfma_i32_16x16x64_i8 v[182:185], v[26:29], v[6:9], v[22:25]
	v_and_b32_e32 v6, v37, v1
	v_and_b32_e32 v7, v37, v150
	v_and_b32_e32 v8, v37, v151
	v_and_b32_e32 v9, v37, v152
	v_mfma_i32_16x16x64_i8 v[178:181], v[18:21], v[10:13], v[30:33]
	v_lshl_add_u64 v[10:11], v[142:143], 0, s[6:7]
	v_lshl_add_u64 v[12:13], v[144:145], 0, s[6:7]
	global_load_dword v171, v[10:11], off
	global_load_dword v172, v[10:11], off offset:256
	global_load_dword v166, v[12:13], off
	global_load_dword v165, v[12:13], off offset:256
	s_waitcnt vmcnt(20)
	v_mfma_i32_16x16x64_i8 v[186:189], v[6:9], v[2:5], v[14:17]
	ds_read2_b32 v[2:3], v164 offset0:128 offset1:132
	ds_read2_b32 v[4:5], v164 offset0:136 offset1:140
	s_lshl_b64 s[6:7], s[40:41], 12
	s_waitcnt lgkmcnt(1)
	v_add_u32_e32 v2, v2, v153
	v_add_u32_e32 v3, v3, v153
	global_load_dwordx4 v[98:101], v2, s[38:39]
	global_load_dwordx4 v[74:77], v3, s[38:39]
	s_waitcnt lgkmcnt(0)
	v_add_u32_e32 v4, v4, v153
	ds_read2_b32 v[2:3], v164 offset0:144 offset1:148
	v_add_u32_e32 v5, v5, v153
	global_load_dwordx4 v[82:85], v4, s[38:39]
	global_load_dwordx4 v[54:57], v5, s[38:39]
	ds_read2_b32 v[4:5], v164 offset0:152 offset1:156
	s_waitcnt lgkmcnt(1)
	v_add_u32_e32 v2, v2, v153
	v_add_u32_e32 v3, v3, v153
	global_load_dwordx4 v[50:53], v2, s[38:39]
	global_load_dwordx4 v[38:41], v3, s[38:39]
	s_waitcnt lgkmcnt(0)
	v_add_u32_e32 v4, v4, v153
	ds_read2_b32 v[2:3], v164 offset0:160 offset1:164
	v_add_u32_e32 v5, v5, v153
	global_load_dwordx4 v[46:49], v4, s[38:39]
	global_load_dwordx4 v[30:33], v5, s[38:39]
	ds_read2_b32 v[4:5], v164 offset0:168 offset1:172
	s_waitcnt lgkmcnt(1)
	v_add_u32_e32 v2, v2, v153
	v_add_u32_e32 v3, v3, v153
	global_load_dwordx4 v[34:37], v2, s[38:39]
	global_load_dwordx4 v[26:29], v3, s[38:39]
	s_waitcnt lgkmcnt(0)
	v_add_u32_e32 v4, v4, v153
	ds_read2_b32 v[2:3], v164 offset0:176 offset1:180
	v_add_u32_e32 v5, v5, v153
	global_load_dwordx4 v[22:25], v4, s[38:39]
	global_load_dwordx4 v[14:17], v5, s[38:39]
	ds_read2_b32 v[4:5], v164 offset0:184 offset1:188
	s_waitcnt lgkmcnt(1)
	v_add_u32_e32 v2, v2, v153
	v_add_u32_e32 v3, v3, v153
	global_load_dwordx4 v[18:21], v2, s[38:39]
	global_load_dwordx4 v[10:13], v3, s[38:39]
	s_waitcnt lgkmcnt(0)
	v_add_u32_e32 v2, v4, v153
	v_add_u32_e32 v3, v5, v153
	global_load_dwordx4 v[6:9], v2, s[38:39]
	s_nop 0
	global_load_dwordx4 v[2:5], v3, s[38:39]
	ds_read_b128 v[190:193], v163 offset:1280
	s_waitcnt lgkmcnt(0)
	v_and_b32_e32 v194, v190, v1
	v_and_b32_e32 v195, v190, v150
	v_and_b32_e32 v196, v190, v151
	v_and_b32_e32 v197, v190, v152
	s_waitcnt vmcnt(35)
	s_nop 0
	v_mfma_i32_16x16x64_i8 v[122:125], v[194:197], v[122:125], v[174:177]
	s_nop 2
	v_and_b32_e32 v174, v191, v1
	v_and_b32_e32 v175, v191, v150
	v_and_b32_e32 v176, v191, v151
	v_and_b32_e32 v177, v191, v152
	s_waitcnt vmcnt(34)
	s_nop 0
	v_mfma_i32_16x16x64_i8 v[118:121], v[174:177], v[118:121], v[178:181]
	v_and_b32_e32 v174, v192, v1
	v_and_b32_e32 v175, v192, v150
	v_and_b32_e32 v176, v192, v151
	v_and_b32_e32 v177, v192, v152
	ds_read_b128 v[178:181], v163 offset:1296
	s_waitcnt vmcnt(33)
	v_mfma_i32_16x16x64_i8 v[126:129], v[174:177], v[126:129], v[182:185]
	v_and_b32_e32 v174, v193, v1
	v_and_b32_e32 v175, v193, v150
	v_and_b32_e32 v176, v193, v151
	v_and_b32_e32 v177, v193, v152
	s_waitcnt vmcnt(32)
	s_nop 0
	v_mfma_i32_16x16x64_i8 v[90:93], v[174:177], v[90:93], v[186:189]
	s_waitcnt lgkmcnt(0)
	v_and_b32_e32 v174, v178, v1
	v_and_b32_e32 v175, v178, v150
	v_and_b32_e32 v176, v178, v151
	v_and_b32_e32 v177, v178, v152
	s_waitcnt vmcnt(31)
	s_nop 0
	v_mfma_i32_16x16x64_i8 v[106:109], v[174:177], v[106:109], v[122:125]
	s_nop 2
	v_and_b32_e32 v122, v179, v1
	v_and_b32_e32 v123, v179, v150
	v_and_b32_e32 v124, v179, v151
	v_and_b32_e32 v125, v179, v152
	s_waitcnt vmcnt(30)
	s_nop 0
	v_mfma_i32_16x16x64_i8 v[86:89], v[122:125], v[86:89], v[118:121]
	ds_read_b128 v[122:125], v163 offset:1312
	s_nop 1
	v_and_b32_e32 v118, v180, v1
	v_and_b32_e32 v119, v180, v150
	v_and_b32_e32 v120, v180, v151
	v_and_b32_e32 v121, v180, v152
	s_waitcnt vmcnt(29)
	s_nop 0
	v_mfma_i32_16x16x64_i8 v[110:113], v[118:121], v[110:113], v[126:129]
	v_and_b32_e32 v118, v181, v1
	v_and_b32_e32 v119, v181, v150
	v_and_b32_e32 v120, v181, v151
	v_and_b32_e32 v121, v181, v152
	s_waitcnt vmcnt(28)
	s_nop 0
	v_mfma_i32_16x16x64_i8 v[78:81], v[118:121], v[78:81], v[90:93]
	s_waitcnt lgkmcnt(0)
	s_nop 1
	v_and_b32_e32 v90, v122, v1
	v_and_b32_e32 v91, v122, v150
	v_and_b32_e32 v92, v122, v151
	v_and_b32_e32 v93, v122, v152
	s_waitcnt vmcnt(27)
	s_nop 0
	v_mfma_i32_16x16x64_i8 v[90:93], v[90:93], v[102:105], v[106:109]
	v_and_b32_e32 v102, v123, v1
	v_and_b32_e32 v103, v123, v150
	v_and_b32_e32 v104, v123, v151
	v_and_b32_e32 v105, v123, v152
	ds_read_b128 v[106:109], v163 offset:1328
	s_waitcnt vmcnt(26)
; #define LAS __attribute__((address_space(3)))
; __device__ __forceinline__ void peer_stage_lists(const PeerMeta& m, LAS int* es, LAS unsigned* crep, LAS float* scp, int lane) {
;     es[lane] = m.e[0] << 8; es[64 + lane] = m.e[1] << 8;
;     const float cmax = wave_max(fmaxf(fabsf(m.c[0]), fabsf(m.c[1])));
;     const float inv = cmax > 0.f ? 127.0f / cmax : 0.f;
;     if (lane == 0) scp[0] = cmax * (1.0f / 127.0f);
	v_mfma_i32_16x16x64_i8 v[86:89], v[102:105], v[94:97], v[86:89]
	v_and_b32_e32 v102, v125, v1
	v_and_b32_e32 v103, v125, v150
	v_and_b32_e32 v104, v125, v151
	v_and_b32_e32 v105, v125, v152
	v_and_b32_e32 v94, v124, v1
	v_and_b32_e32 v95, v124, v150
	s_waitcnt vmcnt(24)
	v_mfma_i32_16x16x64_i8 v[66:69], v[102:105], v[66:69], v[78:81]
	v_and_b32_e32 v96, v124, v151
	s_waitcnt lgkmcnt(0)
	s_nop 0
	v_and_b32_e32 v78, v106, v1
	v_and_b32_e32 v79, v106, v150
	v_and_b32_e32 v80, v106, v151
	v_and_b32_e32 v81, v106, v152
	v_and_b32_e32 v97, v124, v152
	s_waitcnt vmcnt(23)
	v_mfma_i32_16x16x64_i8 v[174:177], v[78:81], v[70:73], v[90:93]
	v_and_b32_e32 v70, v107, v1
	v_and_b32_e32 v71, v107, v150
	v_and_b32_e32 v72, v107, v151
	v_and_b32_e32 v73, v107, v152
	v_mfma_i32_16x16x64_i8 v[94:97], v[94:97], v[114:117], v[110:113]
	s_waitcnt vmcnt(22)
	v_mfma_i32_16x16x64_i8 v[178:181], v[70:73], v[62:65], v[86:89]
	v_and_b32_e32 v62, v108, v1
	v_and_b32_e32 v63, v108, v150
	v_and_b32_e32 v64, v108, v151
	v_and_b32_e32 v65, v108, v152
	s_waitcnt vmcnt(21)
	s_nop 0
	v_mfma_i32_16x16x64_i8 v[182:185], v[62:65], v[58:61], v[94:97]
	v_and_b32_e32 v58, v109, v1
	v_and_b32_e32 v59, v109, v150
	v_and_b32_e32 v60, v109, v151
	v_and_b32_e32 v61, v109, v152
	s_waitcnt vmcnt(20)
	s_nop 0
	v_mfma_i32_16x16x64_i8 v[186:189], v[58:61], v[42:45], v[66:69]
	ds_read2_b32 v[42:43], v164 offset0:192 offset1:196
	ds_read2_b32 v[44:45], v164 offset0:200 offset1:204
	v_add_u32_e32 v176, v176, v180
	v_add_u32_e32 v174, v174, v178
	s_nop 3
	v_add3_u32 v178, v176, v188, v184
	s_waitcnt lgkmcnt(1)
	v_add_u32_e32 v42, v42, v153
	v_add_u32_e32 v43, v43, v153
	global_load_dwordx4 v[126:129], v42, s[38:39]
	global_load_dwordx4 v[118:121], v43, s[38:39]
	s_waitcnt lgkmcnt(0)
	v_add_u32_e32 v44, v44, v153
	ds_read2_b32 v[42:43], v164 offset0:208 offset1:212
	v_add_u32_e32 v45, v45, v153
	global_load_dwordx4 v[122:125], v44, s[38:39]
	global_load_dwordx4 v[114:117], v45, s[38:39]
	ds_read2_b32 v[44:45], v164 offset0:216 offset1:220
	v_add3_u32 v180, v174, v186, v182
	s_waitcnt lgkmcnt(1)
	v_add_u32_e32 v42, v42, v153
	v_add_u32_e32 v43, v43, v153
	global_load_dwordx4 v[110:113], v42, s[38:39]
	global_load_dwordx4 v[102:105], v43, s[38:39]
	s_waitcnt lgkmcnt(0)
	v_add_u32_e32 v44, v44, v153
	ds_read2_b32 v[42:43], v164 offset0:224 offset1:228
	v_add_u32_e32 v45, v45, v153
	global_load_dwordx4 v[106:109], v44, s[38:39]
	global_load_dwordx4 v[86:89], v45, s[38:39]
	ds_read2_b32 v[44:45], v164 offset0:232 offset1:236
	v_add_u32_e32 v177, v177, v181
	s_waitcnt lgkmcnt(1)
	v_add_u32_e32 v42, v42, v153
	v_add_u32_e32 v43, v43, v153
	global_load_dwordx4 v[94:97], v42, s[38:39]
	global_load_dwordx4 v[78:81], v43, s[38:39]
	s_waitcnt lgkmcnt(0)
	v_add_u32_e32 v44, v44, v153
	ds_read2_b32 v[42:43], v164 offset0:240 offset1:244
	v_add_u32_e32 v45, v45, v153
	global_load_dwordx4 v[90:93], v44, s[38:39]
	global_load_dwordx4 v[70:73], v45, s[38:39]
	ds_read2_b32 v[44:45], v164 offset0:248 offset1:252
	v_cvt_f32_i32_e32 v178, v178
	s_waitcnt lgkmcnt(1)
	v_add_u32_e32 v42, v42, v153
	v_add_u32_e32 v43, v43, v153
	global_load_dwordx4 v[66:69], v42, s[38:39]
	global_load_dwordx4 v[62:65], v43, s[38:39]
	s_waitcnt lgkmcnt(0)
	v_add_u32_e32 v42, v44, v153
	v_add_u32_e32 v43, v45, v153
	global_load_dwordx4 v[58:61], v42, s[38:39]
	s_nop 0
	global_load_dwordx4 v[42:45], v43, s[38:39]
	ds_read_b32 v190, v173 offset:2048
	v_add_u32_e32 v173, v175, v179
	v_max_f32_e64 v175, |v167|, |v167|
	v_max_f32_e64 v179, |v168|, |v168|
	v_max_f32_e32 v175, v179, v175
	s_nop 1
	v_add3_u32 v173, v173, v187, v183
	s_waitcnt lgkmcnt(0)
	s_nop 0
	v_max_f32_dpp v175, v175, v175 quad_perm:[1,0,3,2] row_mask:0xf bank_mask:0xf
	s_nop 1
	v_add3_u32 v179, v177, v189, v185
	v_cvt_f32_i32_e32 v177, v173
	v_cvt_f32_i32_e32 v179, v179
	s_waitcnt lgkmcnt(0)
	s_nop 0
	v_max_f32_dpp v181, v175, v175 quad_perm:[2,3,0,1] row_mask:0xf bank_mask:0xf
	s_nop 1
	v_cvt_f32_i32_e32 v176, v180
	v_pk_mul_f32 v[178:179], v[190:191], v[178:179] op_sel_hi:[0,1]
	v_lshl_add_u64 v[174:175], v[148:149], 0, s[6:7]
	s_waitcnt lgkmcnt(0)
	s_nop 0
	v_max_f32_dpp v173, v181, v181 row_half_mirror row_mask:0xf bank_mask:0xf
	s_nop 1
	v_pk_mul_f32 v[176:177], v[190:191], v[176:177] op_sel_hi:[0,1]
	v_cvt_pk_bf16_f32 v176, v176, v177
	s_waitcnt lgkmcnt(0)
	s_nop 0
	v_max_f32_dpp v173, v173, v173 row_mirror row_mask:0xf bank_mask:0xf
	s_nop 1
	v_cvt_pk_bf16_f32 v177, v178, v179
	global_store_dwordx2 v[174:175], v[176:177], off
	s_waitcnt vmcnt(37)
	s_waitcnt lgkmcnt(0)
	s_nop 0
	v_max_f32_dpp v173, v173, v173 row_bcast:15 row_mask:0xa bank_mask:0xf
	s_nop 1
	ds_write2st64_b32 v154, v169, v170 offset1:1
	s_waitcnt lgkmcnt(1)
	s_nop 0
	v_max_f32_dpp v169, v173, v173 row_bcast:31 row_mask:0xc bank_mask:0xf
	s_nop 1
	v_readlane_b32 s98, v169, 63
	s_nop 1
	v_mov_b32_e32 v169, s98
	s_and_saveexec_b64 s[6:7], s[2:3]
	s_cbranch_execz .LBB0_945
	v_mul_f32_e32 v170, 0x3c010204, v169
	v_mov_b32_e32 v173, s11
	ds_write_b32 v173, v170 offset:2048
	s_branch .LBB0_945
